# speedup vs baseline: 1.0012x; 1.0012x over previous
_Z8moe_gemmILi1024ELi2048ELb1EEvPKDF16_S1_PKfPDF16_PfPKiS7_:
	v_lshl_or_b32 v216, s2, 8, v0
	v_and_b32_e32 v217, 63, v216
	v_lshrrev_b32_e32 v216, 6, v216
	v_lshlrev_b32_e32 v215, 3, v217
	v_lshlrev_b32_e32 v214, 4, v217
	v_lshl_add_u32 v217, v216, 10, v215
	v_lshl_add_u32 v216, v216, 11, v214
	s_mov_b32 s96, 16
	s_mov_b32 s97, 0
	s_mov_b32 s98, 0
	s_and_b32 s90, s2, 7
	s_lshr_b32 s91, s2, 3
	v_readfirstlane_b32 s88, v0
	s_load_dwordx2 s[4:5], s[0:1], 0x28
	v_readfirstlane_b32 s12, v0
	s_waitcnt lgkmcnt(0)
	s_load_dwordx2 s[92:93], s[4:5], 0x400
	s_add_u32 s94, s4, 0x6000000
	s_addc_u32 s95, s5, 0
	s_load_dword s23, s[4:5], 0x0
	s_load_dword s25, s[4:5], 0x80
	s_load_dword s27, s[4:5], 0x100
	s_load_dword s29, s[4:5], 0x180
	s_load_dword s31, s[4:5], 0x200
	s_load_dword s33, s[4:5], 0x280
	s_load_dword s35, s[4:5], 0x300
	s_load_dword s38, s[4:5], 0x380
	s_waitcnt lgkmcnt(0)
	global_load_dwordx4 v[218:221], v216, s[92:93] nt
	global_load_dwordx4 v[222:225], v216, s[92:93] offset:1024 nt
	s_add_u32 s92, s92, 0x400000
	s_addc_u32 s93, s93, 0
	global_load_dwordx4 v[226:229], v216, s[92:93] nt
	global_load_dwordx4 v[230:233], v216, s[92:93] offset:1024 nt
	s_add_u32 s92, s92, 0x400000
	s_addc_u32 s93, s93, 0
	global_load_dwordx4 v[234:237], v216, s[92:93] nt
	global_load_dwordx4 v[238:241], v216, s[92:93] offset:1024 nt
	s_add_u32 s92, s92, 0x400000
	s_addc_u32 s93, s93, 0
	global_load_dwordx4 v[242:245], v216, s[92:93] nt
	global_load_dwordx4 v[246:249], v216, s[92:93] offset:1024 nt
	s_add_u32 s92, s92, 0x400000
	s_addc_u32 s93, s93, 0
	s_mov_b32 s100, 1
	s_add_i32 s3, s23, 0x9f
	s_mul_hi_i32 s3, s3, 0x66666667
	s_lshr_b32 s4, s3, 31
	s_ashr_i32 s39, s3, 6
	s_add_i32 s3, s25, 0x9f
	s_mul_hi_i32 s3, s3, 0x66666667
	s_add_i32 s39, s39, s4
	s_lshr_b32 s4, s3, 31
	s_ashr_i32 s40, s3, 6
	s_add_i32 s40, s40, s4
	s_add_i32 s4, s27, 0x9f
	s_mul_hi_i32 s4, s4, 0x66666667
	s_lshr_b32 s5, s4, 31
	s_ashr_i32 s41, s4, 6
	s_add_i32 s4, s29, 0x9f
	s_mul_hi_i32 s4, s4, 0x66666667
	s_add_i32 s41, s41, s5
	s_lshr_b32 s5, s4, 31
	s_ashr_i32 s42, s4, 6
	s_add_i32 s4, s31, 0x9f
	s_mul_hi_i32 s4, s4, 0x66666667
	s_add_i32 s42, s42, s5
	s_lshr_b32 s5, s4, 31
	s_ashr_i32 s43, s4, 6
	s_add_i32 s4, s33, 0x9f
	s_mul_hi_i32 s4, s4, 0x66666667
	s_add_i32 s3, s40, s39
	s_add_i32 s43, s43, s5
	s_lshr_b32 s5, s4, 31
	s_ashr_i32 s44, s4, 6
	s_add_i32 s4, s35, 0x9f
	s_add_i32 s3, s41, s3
	s_mul_hi_i32 s4, s4, 0x66666667
	s_add_i32 s3, s42, s3
	s_add_i32 s44, s44, s5
	s_lshr_b32 s5, s4, 31
	s_ashr_i32 s45, s4, 6
	s_add_i32 s4, s38, 0x9f
	s_add_i32 s3, s43, s3
	s_mul_hi_i32 s4, s4, 0x66666667
	s_add_i32 s3, s44, s3
	s_add_i32 s45, s45, s5
	s_lshr_b32 s5, s4, 31
	s_ashr_i32 s46, s4, 6
	s_add_i32 s3, s45, s3
	s_add_i32 s46, s46, s5
	s_add_i32 s3, s46, s3
	s_lshl_b32 s3, s3, 4
	s_and_b32 s4, s2, 7
	s_mul_i32 s4, s3, s4
	s_lshr_b32 s2, s2, 3
	s_ashr_i32 s5, s4, 3
	s_add_i32 s4, s4, s3
	s_ashr_i32 s47, s4, 3
	s_add_i32 s48, s5, s2
	s_sub_i32 s89, s47, s5
	s_sub_i32 s89, s89, 64
	s_max_i32 s89, s89, 0
	s_min_i32 s89, s89, 64
	s_add_i32 s99, s48, 64
	s_cmp_lt_i32 s99, s47
	s_cselect_b32 s98, 1, 0
	s_cmp_eq_u32 s98, 0
	s_cbranch_scc1 .Las_set
	s_cmp_ge_i32 s89, 64
	s_cbranch_scc1 .Las_set
	s_mov_b32 s96, 8
	s_mov_b32 s98, 1
